# prologue/epilogue de-serialisation: the attention unit epilogue issues its 8 LDS reads of the staged O rows together and then 8 write-through stores behind counted waits (was a read-wait-store ladder)
# speedup vs baseline: 1.0035x; 1.0020x over previous
; #define SBAR() __builtin_amdgcn_sched_barrier(0)
; __device__ __forceinline__ int crow(int r, int hi) { return (r & 3) + 8 * (r >> 2) + 4 * hi; }
; #define RESC(a) do { if (__any((a) < 1.f)) { if (hi == 0) al_l[r32] = (a); asm volatile("s_waitcnt lgkmcnt(0)" ::: "memory"); \
;     for (int d = 0; d < 4; ++d) for (int r = 0; r < 16; ++r) o[d][r] *= al_l[crow(r, hi)]; } } while (0)
; #define RESC(a) do { if (__any((a) < 1.f)) { if (hi == 0) al_l[r32] = (a); asm volatile("s_waitcnt lgkmcnt(0)" ::: "memory"); \
;     for (int d = 0; d < 4; ++d) for (int r = 0; r < 16; ++r) o[d][r] *= al_l[crow(r, hi)]; } } while (0)
; __device__ __forceinline__ void attn_dma_body(const bf16_t* __restrict__ Qb, int ldq, int tpos0, const float* __restrict__ rope, const float* __restrict__ qgain, ...
;     ...
;   { SBAR(); qkt(pB0, pB1, (const bf16_t*)(lds + ((NT - 1) & 3) * SHM_SLOT), qr, r32, hi);
;     finishSM(pA0, pA1, alA, l_reg, pa0, pa1, pa2, pa3); SBAR();
;     pv_d0(o, vb0 + ((NT - 2) & 3) * (int)SHM_SLOT, pa0, pa1, pa2, pa3); partialSM(pB0, pB1, m_reg, mnB, alB);
;     RESC(alB);
;     finishSM(pB0, pB1, alB, l_reg, pa0, pa1, pa2, pa3); SBAR();
;     pv_d0(o, vb0 + ((NT - 1) & 3) * (int)SHM_SLOT, pa0, pa1, pa2, pa3); }
;   if (hi == 0) li_l[r32] = l_reg; asm volatile("s_waitcnt lgkmcnt(0)" ::: "memory");
;   float rli[16];
; #pragma unroll
;   for (int r = 0; r < 16; ++r) rli[r] = __builtin_amdgcn_rcpf(li_l[crow(r, hi)]);
;   bf16_t* Ow = Ob + (long)(wid * QBLK) * LDO;
;   asm volatile("s_waitcnt lgkmcnt(0)\n\ts_barrier" ::: "memory");
.Lf16_done:
	s_mov_b32 s37, 0x18000
	ds_read_b64_tr_b16 v[214:215], v180 offset:32768
	ds_read_b64_tr_b16 v[216:217], v180 offset:36864
	ds_read_b64_tr_b16 v[218:219], v181 offset:32768
	ds_read_b64_tr_b16 v[220:221], v181 offset:36864
	ds_read_b64_tr_b16 v[222:223], v180 offset:33280
	ds_read_b64_tr_b16 v[224:225], v180 offset:37376
	ds_read_b64_tr_b16 v[226:227], v181 offset:33280
	ds_read_b64_tr_b16 v[228:229], v181 offset:37376
	ds_read_b64_tr_b16 v[230:231], v180 offset:33792
	ds_read_b64_tr_b16 v[232:233], v180 offset:37888
	ds_read_b64_tr_b16 v[234:235], v181 offset:33792
	ds_read_b64_tr_b16 v[236:237], v181 offset:37888
	s_waitcnt lgkmcnt(8)
	v_mfma_f32_16x16x32_bf16 v[2:5], v[214:217], v[130:133], v[2:5]
	v_mfma_f32_16x16x32_bf16 v[6:9], v[214:217], v[138:141], v[6:9]
	v_mfma_f32_16x16x32_bf16 v[10:13], v[218:221], v[130:133], v[10:13]
	v_mfma_f32_16x16x32_bf16 v[14:17], v[218:221], v[138:141], v[14:17]
	ds_read_b64_tr_b16 v[238:239], v180 offset:34304
	ds_read_b64_tr_b16 v[240:241], v180 offset:38400
	ds_read_b64_tr_b16 v[242:243], v181 offset:34304
	ds_read_b64_tr_b16 v[244:245], v181 offset:38400
	s_waitcnt lgkmcnt(8)
	v_mfma_f32_16x16x32_bf16 v[18:21], v[222:225], v[130:133], v[18:21]
	v_mfma_f32_16x16x32_bf16 v[22:25], v[222:225], v[138:141], v[22:25]
	v_mfma_f32_16x16x32_bf16 v[26:29], v[226:229], v[130:133], v[26:29]
	v_mfma_f32_16x16x32_bf16 v[30:33], v[226:229], v[138:141], v[30:33]
	v_mfma_f32_16x16x32_bf16 v[246:249], v[194:197], v[130:133], v[246:249]
	ds_read_b64_tr_b16 v[214:215], v180 offset:40960
	ds_read_b64_tr_b16 v[216:217], v180 offset:45056
	ds_read_b64_tr_b16 v[218:219], v181 offset:40960
	ds_read_b64_tr_b16 v[220:221], v181 offset:45056
	s_waitcnt lgkmcnt(8)
	v_mfma_f32_16x16x32_bf16 v[34:37], v[230:233], v[130:133], v[34:37]
	v_mfma_f32_16x16x32_bf16 v[38:41], v[230:233], v[138:141], v[38:41]
	v_mfma_f32_16x16x32_bf16 v[42:45], v[234:237], v[130:133], v[42:45]
	v_mfma_f32_16x16x32_bf16 v[46:49], v[234:237], v[138:141], v[46:49]
	ds_read_b64_tr_b16 v[222:223], v180 offset:41472
	ds_read_b64_tr_b16 v[224:225], v180 offset:45568
	ds_read_b64_tr_b16 v[226:227], v181 offset:41472
	ds_read_b64_tr_b16 v[228:229], v181 offset:45568
	s_waitcnt lgkmcnt(8)
	v_mfma_f32_16x16x32_bf16 v[50:53], v[238:241], v[130:133], v[50:53]
	v_mfma_f32_16x16x32_bf16 v[54:57], v[238:241], v[138:141], v[54:57]
	v_mfma_f32_16x16x32_bf16 v[58:61], v[242:245], v[130:133], v[58:61]
	v_mfma_f32_16x16x32_bf16 v[62:65], v[242:245], v[138:141], v[62:65]
	v_mfma_f32_16x16x32_bf16 v[252:255], v[194:197], v[138:141], v[252:255]
	ds_read_b64_tr_b16 v[230:231], v180 offset:41984
	ds_read_b64_tr_b16 v[232:233], v180 offset:46080
	ds_read_b64_tr_b16 v[234:235], v181 offset:41984
	ds_read_b64_tr_b16 v[236:237], v181 offset:46080
	s_waitcnt lgkmcnt(8)
	v_mfma_f32_16x16x32_bf16 v[2:5], v[214:217], v[134:137], v[2:5]
	v_mfma_f32_16x16x32_bf16 v[6:9], v[214:217], v[142:145], v[6:9]
	v_mfma_f32_16x16x32_bf16 v[10:13], v[218:221], v[134:137], v[10:13]
	v_mfma_f32_16x16x32_bf16 v[14:17], v[218:221], v[142:145], v[14:17]
	ds_read_b64_tr_b16 v[238:239], v180 offset:42496
	ds_read_b64_tr_b16 v[240:241], v180 offset:46592
	ds_read_b64_tr_b16 v[242:243], v181 offset:42496
	ds_read_b64_tr_b16 v[244:245], v181 offset:46592
	s_waitcnt lgkmcnt(8)
	v_mfma_f32_16x16x32_bf16 v[18:21], v[222:225], v[134:137], v[18:21]
	v_mfma_f32_16x16x32_bf16 v[22:25], v[222:225], v[142:145], v[22:25]
	v_mfma_f32_16x16x32_bf16 v[26:29], v[226:229], v[134:137], v[26:29]
	v_mfma_f32_16x16x32_bf16 v[30:33], v[226:229], v[142:145], v[30:33]
	v_mfma_f32_16x16x32_bf16 v[246:249], v[194:197], v[134:137], v[246:249]
	s_waitcnt lgkmcnt(4)
	v_mfma_f32_16x16x32_bf16 v[34:37], v[230:233], v[134:137], v[34:37]
	v_mfma_f32_16x16x32_bf16 v[38:41], v[230:233], v[142:145], v[38:41]
	v_mfma_f32_16x16x32_bf16 v[42:45], v[234:237], v[134:137], v[42:45]
	v_mfma_f32_16x16x32_bf16 v[46:49], v[234:237], v[142:145], v[46:49]
	s_waitcnt lgkmcnt(0)
	v_mfma_f32_16x16x32_bf16 v[50:53], v[238:241], v[134:137], v[50:53]
	v_mfma_f32_16x16x32_bf16 v[54:57], v[238:241], v[142:145], v[54:57]
	v_mfma_f32_16x16x32_bf16 v[58:61], v[242:245], v[134:137], v[58:61]
	v_mfma_f32_16x16x32_bf16 v[62:65], v[242:245], v[142:145], v[62:65]
	v_mfma_f32_16x16x32_bf16 v[252:255], v[194:197], v[142:145], v[252:255]
	s_nop 7
	s_nop 7
	v_mov_b32_e32 v182, v246
	v_mov_b32_e32 v195, v252
	v_rcp_f32_e32 v182, v182
	v_rcp_f32_e32 v195, v195
	s_waitcnt lgkmcnt(0)
	s_barrier
; __device__ __forceinline__ unsigned f2bf(float f) { unsigned u = __builtin_bit_cast(unsigned, f); return (u + 0x7fffu + ((u >> 16) & 1u)) >> 16; }
; __device__ __forceinline__ int crow(int r, int hi) { return (r & 3) + 8 * (r >> 2) + 4 * hi; }
; #define ATT_WAIT_BAR() asm volatile("s_waitcnt vmcnt(0) lgkmcnt(0)\n\ts_barrier" ::: "memory")
; __device__ __forceinline__ void attn_dma_body(const bf16_t* __restrict__ Qb, int ldq, int tpos0, const float* __restrict__ rope, const float* __restrict__ qgain, ...
;     ...
;   { char* st = lds + wid * 8704;
; #pragma unroll
;     for (int r = 0; r < 16; ++r) { const int orow = crow(r, hi);
; #pragma unroll
;       for (int d0 = 0; d0 < 4; ++d0) *(bf16_t*)(st + orow * 272 + (d0 * 32 + r32) * 2) = (bf16_t)f2bf(o[d0][r] * rli[r]); }
;     asm volatile("s_waitcnt lgkmcnt(0)" ::: "memory");
; #pragma unroll
;     for (int i = 0; i < 8; ++i) { const int c = i * 64 + lane, row = c >> 4, cc = c & 15; const u32x4 v = *(const u32x4*)(st + row * 272 + cc * 16);
;       const bf16_t* gp = Ow + (long)row * LDO + cc * 8;
;       asm volatile("global_store_dwordx4 %0, %1, off sc1\n\ts_nop 1" :: "v"(gp), "v"(v) : "memory"); } }
;   ATT_WAIT_BAR();
	v_mul_u32_u24_e32 v84, 0x2200, v179
	v_and_b32_e32 v246, 15, v167
	v_lshrrev_b32_e32 v247, 4, v167
	v_mul_u32_u24_e32 v248, 0x110, v246
	v_add_u32_e32 v248, v248, v84
	v_lshl_add_u32 v248, v247, 3, v248
	v_mul_f32_e32 v2, v2, v182
	v_mul_f32_e32 v3, v3, v182
	v_mul_f32_e32 v4, v4, v182
	v_mul_f32_e32 v5, v5, v182
	v_cvt_pk_bf16_f32 v252, v2, v3
	v_cvt_pk_bf16_f32 v253, v4, v5
	ds_write_b64 v248, v[252:253] offset:0
	v_mul_f32_e32 v6, v6, v195
	v_mul_f32_e32 v7, v7, v195
	v_mul_f32_e32 v8, v8, v195
	v_mul_f32_e32 v9, v9, v195
	v_cvt_pk_bf16_f32 v254, v6, v7
	v_cvt_pk_bf16_f32 v255, v8, v9
	ds_write_b64 v248, v[254:255] offset:4352
	v_mul_f32_e32 v10, v10, v182
	v_mul_f32_e32 v11, v11, v182
	v_mul_f32_e32 v12, v12, v182
	v_mul_f32_e32 v13, v13, v182
	v_cvt_pk_bf16_f32 v252, v10, v11
	v_cvt_pk_bf16_f32 v253, v12, v13
	ds_write_b64 v248, v[252:253] offset:32
	v_mul_f32_e32 v14, v14, v195
	v_mul_f32_e32 v15, v15, v195
	v_mul_f32_e32 v16, v16, v195
	v_mul_f32_e32 v17, v17, v195
	v_cvt_pk_bf16_f32 v254, v14, v15
	v_cvt_pk_bf16_f32 v255, v16, v17
	ds_write_b64 v248, v[254:255] offset:4384
	v_mul_f32_e32 v18, v18, v182
	v_mul_f32_e32 v19, v19, v182
	v_mul_f32_e32 v20, v20, v182
	v_mul_f32_e32 v21, v21, v182
	v_cvt_pk_bf16_f32 v252, v18, v19
	v_cvt_pk_bf16_f32 v253, v20, v21
	ds_write_b64 v248, v[252:253] offset:64
	v_mul_f32_e32 v22, v22, v195
	v_mul_f32_e32 v23, v23, v195
	v_mul_f32_e32 v24, v24, v195
	v_mul_f32_e32 v25, v25, v195
	v_cvt_pk_bf16_f32 v254, v22, v23
	v_cvt_pk_bf16_f32 v255, v24, v25
	ds_write_b64 v248, v[254:255] offset:4416
	v_mul_f32_e32 v26, v26, v182
	v_mul_f32_e32 v27, v27, v182
	v_mul_f32_e32 v28, v28, v182
	v_mul_f32_e32 v29, v29, v182
	v_cvt_pk_bf16_f32 v252, v26, v27
	v_cvt_pk_bf16_f32 v253, v28, v29
	ds_write_b64 v248, v[252:253] offset:96
	v_mul_f32_e32 v30, v30, v195
	v_mul_f32_e32 v31, v31, v195
	v_mul_f32_e32 v32, v32, v195
	v_mul_f32_e32 v33, v33, v195
	v_cvt_pk_bf16_f32 v254, v30, v31
	v_cvt_pk_bf16_f32 v255, v32, v33
	ds_write_b64 v248, v[254:255] offset:4448
	v_mul_f32_e32 v34, v34, v182
	v_mul_f32_e32 v35, v35, v182
	v_mul_f32_e32 v36, v36, v182
	v_mul_f32_e32 v37, v37, v182
	v_cvt_pk_bf16_f32 v252, v34, v35
	v_cvt_pk_bf16_f32 v253, v36, v37
	ds_write_b64 v248, v[252:253] offset:128
	v_mul_f32_e32 v38, v38, v195
	v_mul_f32_e32 v39, v39, v195
	v_mul_f32_e32 v40, v40, v195
	v_mul_f32_e32 v41, v41, v195
	v_cvt_pk_bf16_f32 v254, v38, v39
	v_cvt_pk_bf16_f32 v255, v40, v41
	ds_write_b64 v248, v[254:255] offset:4480
	v_mul_f32_e32 v42, v42, v182
	v_mul_f32_e32 v43, v43, v182
	v_mul_f32_e32 v44, v44, v182
	v_mul_f32_e32 v45, v45, v182
	v_cvt_pk_bf16_f32 v252, v42, v43
	v_cvt_pk_bf16_f32 v253, v44, v45
	ds_write_b64 v248, v[252:253] offset:160
	v_mul_f32_e32 v46, v46, v195
	v_mul_f32_e32 v47, v47, v195
	v_mul_f32_e32 v48, v48, v195
	v_mul_f32_e32 v49, v49, v195
	v_cvt_pk_bf16_f32 v254, v46, v47
	v_cvt_pk_bf16_f32 v255, v48, v49
	ds_write_b64 v248, v[254:255] offset:4512
	v_mul_f32_e32 v50, v50, v182
	v_mul_f32_e32 v51, v51, v182
	v_mul_f32_e32 v52, v52, v182
	v_mul_f32_e32 v53, v53, v182
	v_cvt_pk_bf16_f32 v252, v50, v51
	v_cvt_pk_bf16_f32 v253, v52, v53
	ds_write_b64 v248, v[252:253] offset:192
	v_mul_f32_e32 v54, v54, v195
	v_mul_f32_e32 v55, v55, v195
	v_mul_f32_e32 v56, v56, v195
	v_mul_f32_e32 v57, v57, v195
	v_cvt_pk_bf16_f32 v254, v54, v55
	v_cvt_pk_bf16_f32 v255, v56, v57
	ds_write_b64 v248, v[254:255] offset:4544
	v_mul_f32_e32 v58, v58, v182
	v_mul_f32_e32 v59, v59, v182
	v_mul_f32_e32 v60, v60, v182
	v_mul_f32_e32 v61, v61, v182
	v_cvt_pk_bf16_f32 v252, v58, v59
	v_cvt_pk_bf16_f32 v253, v60, v61
	ds_write_b64 v248, v[252:253] offset:224
	v_mul_f32_e32 v62, v62, v195
	v_mul_f32_e32 v63, v63, v195
	v_mul_f32_e32 v64, v64, v195
	v_mul_f32_e32 v65, v65, v195
	v_cvt_pk_bf16_f32 v254, v62, v63
	v_cvt_pk_bf16_f32 v255, v64, v65
	ds_write_b64 v248, v[254:255] offset:4576
	s_waitcnt lgkmcnt(0)
	s_lshl_b64 s[6:7], s[70:71], 12
	s_add_u32 s6, s23, s6
	s_addc_u32 s7, s94, s7
	s_add_u32 s6, s6, s44
	s_addc_u32 s7, s7, s45
	v_ashrrev_i32_e32 v165, 31, v164
	v_lshlrev_b64 v[66:67], 12, v[164:165]
	v_lshl_add_u64 v[6:7], s[6:7], 0, v[66:67]
	v_lshlrev_b32_e32 v162, 4, v246
	v_lshl_add_u64 v[6:7], v[6:7], 0, v[162:163]
	v_lshlrev_b32_e32 v162, 12, v247
	v_lshl_add_u64 v[6:7], v[6:7], 0, v[162:163]
	v_mul_u32_u24_e32 v249, 0x110, v247
	v_add_u32_e32 v249, v249, v84
	v_lshl_add_u32 v249, v246, 4, v249
	ds_read_b128 v[66:69], v249 offset:0
	ds_read_b128 v[70:73], v249 offset:1088
	ds_read_b128 v[74:77], v249 offset:2176
	ds_read_b128 v[78:81], v249 offset:3264
	ds_read_b128 v[82:85], v249 offset:4352
	ds_read_b128 v[86:89], v249 offset:5440
	ds_read_b128 v[90:93], v249 offset:6528
	ds_read_b128 v[94:97], v249 offset:7616
	s_mov_b64 s[8:9], 0x0
	v_lshl_add_u64 v[8:9], v[6:7], 0, s[8:9]
	s_waitcnt lgkmcnt(7)
	global_store_dwordx4 v[8:9], v[66:69], off sc1
	s_mov_b64 s[8:9], 0x4000
	v_lshl_add_u64 v[98:99], v[6:7], 0, s[8:9]
	s_waitcnt lgkmcnt(6)
	global_store_dwordx4 v[98:99], v[70:73], off sc1
	s_mov_b64 s[8:9], 0x8000
	v_lshl_add_u64 v[8:9], v[6:7], 0, s[8:9]
	s_waitcnt lgkmcnt(5)
	global_store_dwordx4 v[8:9], v[74:77], off sc1
	s_mov_b64 s[8:9], 0xc000
	v_lshl_add_u64 v[98:99], v[6:7], 0, s[8:9]
	s_waitcnt lgkmcnt(4)
	global_store_dwordx4 v[98:99], v[78:81], off sc1
	s_mov_b64 s[8:9], 0x10000
	v_lshl_add_u64 v[8:9], v[6:7], 0, s[8:9]
	s_waitcnt lgkmcnt(3)
	global_store_dwordx4 v[8:9], v[82:85], off sc1
	s_mov_b64 s[8:9], 0x14000
	v_lshl_add_u64 v[98:99], v[6:7], 0, s[8:9]
	s_waitcnt lgkmcnt(2)
	global_store_dwordx4 v[98:99], v[86:89], off sc1
	s_mov_b64 s[8:9], 0x18000
	v_lshl_add_u64 v[8:9], v[6:7], 0, s[8:9]
	s_waitcnt lgkmcnt(1)
	global_store_dwordx4 v[8:9], v[90:93], off sc1
	s_mov_b64 s[8:9], 0x1c000
	v_lshl_add_u64 v[98:99], v[6:7], 0, s[8:9]
	s_waitcnt lgkmcnt(0)
	global_store_dwordx4 v[98:99], v[94:97], off sc1
	s_waitcnt vmcnt(0) lgkmcnt(0)
	s_barrier
	v_readlane_b32 s96, v250, 4
	v_readlane_b32 s97, v250, 5
	s_setprio 0
	s_branch .LBB0_437
